# waves 0-3 run the whole kernel at s_setprio 1, every per-segment priority flip deleted
# speedup vs baseline: 1.0058x; 1.0004x over previous
; #define LAS __attribute__((address_space(3)))
; #define TID fresh_tid()
; __global__ void __launch_bounds__(NWAVES * 64, 2) fwd(Args args) {
;     extern __shared__ __attribute__((aligned(16))) unsigned char lds_raw[];
;     LAS unsigned char* lds = (LAS unsigned char*)lds_raw;
;     volatile LAS unsigned* MISC = (volatile LAS unsigned*)(lds + MISC_OFF);
;     ...
;     const int wave = __builtin_amdgcn_readfirstlane(TID >> 6);
;     const int G = gridDim.x; const int bx = blockIdx.x; const int vcu = (G % 8 == 0) ? (bx % 8) * (G / 8) + bx / 8 : bx;
;     const int gw = vcu * NWAVES + wave, NGW = G * NWAVES;
_Z3fwd4Args:
	v_mov_b32_e32 v212, v0
	s_load_dwordx2 s[18:19], s[0:1], 0xa0
	s_load_dword s12, s[0:1], 0xa8
	s_load_dwordx8 s[4:11], s[0:1], 0x80
	s_mov_b32 s20, s2
	s_waitcnt lgkmcnt(0)
	v_writelane_b32 v252, s4, 0
	s_nop 1
	v_writelane_b32 v252, s5, 1
	v_writelane_b32 v252, s6, 2
	v_writelane_b32 v252, s7, 3
	v_writelane_b32 v252, s8, 4
	v_writelane_b32 v252, s9, 5
	v_writelane_b32 v252, s10, 6
	v_writelane_b32 v252, s11, 7
	s_add_u32 s4, s0, 0xa8
	s_addc_u32 s5, s1, 0
	v_writelane_b32 v252, s4, 8
	s_and_b32 s3, s12, 7
	v_readfirstlane_b32 s6, v0
	s_nop 3
	s_cmp_lt_u32 s6, 256
	s_cbranch_scc0 .Lgprio_skip
	s_setprio 1
.Lgprio_skip:
	v_writelane_b32 v252, s5, 9
	s_mov_b32 s4, s12
	v_writelane_b32 v252, s4, 10
	s_cmp_lg_u32 s3, 0
	s_nop 0
	v_writelane_b32 v252, s5, 11
	v_writelane_b32 v252, s2, 12
	s_cbranch_scc1 .LBB0_2
	s_load_dword s2, s[0:1], 0xa8
	s_ashr_i32 s3, s20, 31
	s_lshr_b32 s3, s3, 29
	s_add_i32 s3, s20, s3
	s_and_b32 s4, s3, -8
	s_waitcnt lgkmcnt(0)
	s_ashr_i32 s2, s2, 3
	s_sub_i32 s4, s20, s4
	s_mul_i32 s2, s2, s4
	s_ashr_i32 s3, s3, 3
	s_add_i32 s2, s2, s3
	v_writelane_b32 v252, s2, 12
